# E42: grid barrier one hop shorter: non-leader workgroups spin on the global generation word directly, per-XCD XGEN bump + its wait dropped
# baseline (speedup 1.0000x reference)
; __device__ __forceinline__ int lane_id() { unsigned ones = ~0u; asm volatile("" : "+s"(ones)); return (int)__builtin_amdgcn_mbcnt_hi(ones, __builtin_amdgcn_mbcnt_lo(ones, 0u)); }
; __device__ __forceinline__ unsigned xb_ld(unsigned* p)              { return __hip_atomic_load(p, __ATOMIC_RELAXED, __HIP_MEMORY_SCOPE_AGENT); }
; __device__ __forceinline__ unsigned xb_add(unsigned* p, unsigned v) { return __hip_atomic_fetch_add(p, v, __ATOMIC_RELAXED, __HIP_MEMORY_SCOPE_AGENT); }
; __device__ __forceinline__ unsigned xb_xcc_id() { return (unsigned)__builtin_amdgcn_s_getreg((3 << 11) | 20) & 0xFu; }
; #define XB_SPIN(cond, bar) do { unsigned _sp = 0; while (cond) { __builtin_amdgcn_s_sleep(1); \
;     if ((++_sp & 255u) == 0u) { if (xb_ld(&(bar)[XB_TMO])) break; if (_sp > XB_SPIN_CAP) { atomicAdd(&(bar)[XB_TMO], 1u); break; } } } } while (0)
; __device__ __forceinline__ void xcd_barrier(const XcdBarrier& b, int wave_s) {
;     ...
;     if (wave_s == 0 && lane_id() == 0) {
;         unsigned* bar = b.bar; asm volatile("" : "+s"(bar));
;         const unsigned bx_ = xb_xcc_id();
;         __builtin_amdgcn_s_waitcnt(0);
;         unsigned nloc = b.st[0], nx = b.st[1];
;         if (nloc == 0u) { xcd_barrier_complete(bar, bx_, nloc, nx); b.st[0] = nloc; b.st[1] = nx; }
;         const unsigned old = xb_add(&bar[XB_XSUB(bx_)], 1u);
;         const unsigned gen = old / nloc;
;         if (old + 1u == (gen + 1u) * nloc) {
;             __builtin_amdgcn_fence(__ATOMIC_RELEASE, "agent");
;             asm volatile("s_waitcnt vmcnt(0)" ::: "memory");
;             const unsigned og = xb_add(&bar[XB_TOP], 1u);
;             const unsigned tg = og / nx;
;             if (og + 1u == (tg + 1u) * nx) xb_add(&bar[XB_TOPGEN], 1u);
;             else XB_SPIN(xb_ld(&bar[XB_TOPGEN]) == tg, bar);
;             __builtin_amdgcn_fence(__ATOMIC_ACQUIRE, "agent");
;             xb_add(&bar[XB_XGEN(bx_)], 1u);
;             asm volatile("s_waitcnt vmcnt(0)" ::: "memory");
;         } else {
;             XB_SPIN(xb_ld(&bar[XB_XGEN(bx_)]) == gen, bar);
.LBB0_51:
	s_lshl_b32 s2, s33, 8
	s_add_u32 s23, s40, s2
	s_addc_u32 s22, s41, 0
	v_mov_b32_e32 v1, s23
	v_add_co_u32_e32 v4, vcc, 0x1000, v1
	v_mov_b32_e32 v1, s22
	s_nop 0
	v_addc_co_u32_e32 v5, vcc, 0, v1, vcc
	v_mov_b32_e32 v1, 1
	flat_atomic_add v1, v[4:5], v1 offset:1024 sc0
	v_cvt_f32_u32_e32 v3, v2
	v_sub_u32_e32 v4, 0, v2
	v_rcp_iflag_f32_e32 v3, v3
	s_nop 0
	v_mul_f32_e32 v3, 0x4f7ffffe, v3
	v_cvt_u32_f32_e32 v3, v3
	v_mul_lo_u32 v4, v4, v3
	v_mul_hi_u32 v4, v3, v4
	v_add_u32_e32 v3, v3, v4
	s_waitcnt vmcnt(0) lgkmcnt(0)
	v_mul_hi_u32 v3, v1, v3
	v_mul_lo_u32 v5, v3, v2
	v_add_u32_e32 v4, 1, v1
	v_sub_u32_e32 v1, v1, v5
	v_add_u32_e32 v6, 1, v3
	v_cmp_ge_u32_e32 vcc, v1, v2
	v_sub_u32_e32 v5, v1, v2
	s_nop 0
	v_cndmask_b32_e32 v3, v3, v6, vcc
	v_cndmask_b32_e32 v1, v1, v5, vcc
	v_add_u32_e32 v5, 1, v3
	v_cmp_ge_u32_e32 vcc, v1, v2
	s_nop 1
	v_cndmask_b32_e32 v1, v3, v5, vcc
	v_mad_u64_u32 v[2:3], s[2:3], v2, v1, v[2:3]
	v_cmp_ne_u32_e32 vcc, v4, v2
	s_and_saveexec_b64 s[2:3], vcc
	s_xor_b64 s[2:3], exec, s[2:3]
	s_cbranch_execz .LBB0_64
	v_mov_b32_e32 v0, s40
	v_add_co_u32_e32 v2, vcc, 0x3100, v0
	v_mov_b32_e32 v0, s41
	s_nop 0
	v_addc_co_u32_e32 v3, vcc, 0, v0, vcc
	flat_load_dword v0, v[2:3] offset:1024 sc1
	s_add_u32 s6, s40, 0x3500
	s_addc_u32 s7, s41, 0
	s_waitcnt vmcnt(0) lgkmcnt(0)
	v_cmp_eq_u32_e32 vcc, v0, v1
	s_and_saveexec_b64 s[4:5], vcc
	s_cbranch_execz .LBB0_63
	s_mov_b32 s24, 1
	s_mov_b64 s[8:9], 0
	s_branch .LBB0_55

; __device__ __forceinline__ unsigned xb_ld(unsigned* p)              { return __hip_atomic_load(p, __ATOMIC_RELAXED, __HIP_MEMORY_SCOPE_AGENT); }
; __device__ __forceinline__ unsigned xb_add(unsigned* p, unsigned v) { return __hip_atomic_fetch_add(p, v, __ATOMIC_RELAXED, __HIP_MEMORY_SCOPE_AGENT); }
; #define XB_SPIN(cond, bar) do { unsigned _sp = 0; while (cond) { __builtin_amdgcn_s_sleep(1); \
;     if ((++_sp & 255u) == 0u) { if (xb_ld(&(bar)[XB_TMO])) break; if (_sp > XB_SPIN_CAP) { atomicAdd(&(bar)[XB_TMO], 1u); break; } } } } while (0)
; __device__ __forceinline__ void xcd_barrier(const XcdBarrier& b, int wave_s) {
;     ...
;         if (old + 1u == (gen + 1u) * nloc) {
;             __builtin_amdgcn_fence(__ATOMIC_RELEASE, "agent");
;             asm volatile("s_waitcnt vmcnt(0)" ::: "memory");
;             const unsigned og = xb_add(&bar[XB_TOP], 1u);
;             const unsigned tg = og / nx;
;             if (og + 1u == (tg + 1u) * nx) xb_add(&bar[XB_TOPGEN], 1u);
;             else XB_SPIN(xb_ld(&bar[XB_TOPGEN]) == tg, bar);
;             __builtin_amdgcn_fence(__ATOMIC_ACQUIRE, "agent");
;             xb_add(&bar[XB_XGEN(bx_)], 1u);
;             asm volatile("s_waitcnt vmcnt(0)" ::: "memory");
.LBB0_79:
	s_or_b64 exec, exec, s[2:3]
	v_mov_b32_e32 v0, s23
	v_add_co_u32_e32 v0, vcc, 0x2000, v0
	v_mov_b32_e32 v1, s22
	s_nop 0
	v_addc_co_u32_e32 v1, vcc, 0, v1, vcc
	v_mov_b32_e32 v2, 1
	s_waitcnt vmcnt(0) lgkmcnt(0)
	buffer_inv sc1
.LBB0_80:
	s_or_b64 exec, exec, s[36:37]

; __device__ __forceinline__ unsigned xb_ld(unsigned* p)              { return __hip_atomic_load(p, __ATOMIC_RELAXED, __HIP_MEMORY_SCOPE_AGENT); }
; __device__ __forceinline__ unsigned xb_add(unsigned* p, unsigned v) { return __hip_atomic_fetch_add(p, v, __ATOMIC_RELAXED, __HIP_MEMORY_SCOPE_AGENT); }
; #define XB_SPIN(cond, bar) do { unsigned _sp = 0; while (cond) { __builtin_amdgcn_s_sleep(1); \
;     if ((++_sp & 255u) == 0u) { if (xb_ld(&(bar)[XB_TMO])) break; if (_sp > XB_SPIN_CAP) { atomicAdd(&(bar)[XB_TMO], 1u); break; } } } } while (0)
; __device__ __forceinline__ void xcd_barrier(const XcdBarrier& b, int wave_s) {
;     ...
;         if (old + 1u == (gen + 1u) * nloc) {
;             __builtin_amdgcn_fence(__ATOMIC_RELEASE, "agent");
;             asm volatile("s_waitcnt vmcnt(0)" ::: "memory");
;             const unsigned og = xb_add(&bar[XB_TOP], 1u);
;             const unsigned tg = og / nx;
;             if (og + 1u == (tg + 1u) * nx) xb_add(&bar[XB_TOPGEN], 1u);
;             else XB_SPIN(xb_ld(&bar[XB_TOPGEN]) == tg, bar);
;             __builtin_amdgcn_fence(__ATOMIC_ACQUIRE, "agent");
;             xb_add(&bar[XB_XGEN(bx_)], 1u);
;             asm volatile("s_waitcnt vmcnt(0)" ::: "memory");
.LBB0_82:
	s_or_b64 exec, exec, s[2:3]
	v_mov_b32_e32 v0, s23
	v_add_co_u32_e32 v0, vcc, 0x2000, v0
	v_mov_b32_e32 v1, s22
	s_nop 0
	v_addc_co_u32_e32 v1, vcc, 0, v1, vcc
	s_waitcnt vmcnt(0) lgkmcnt(0)
	buffer_inv sc1
.LBB0_83:
	s_or_b64 exec, exec, s[40:41]

; __device__ __forceinline__ int lane_id() { unsigned ones = ~0u; asm volatile("" : "+s"(ones)); return (int)__builtin_amdgcn_mbcnt_hi(ones, __builtin_amdgcn_mbcnt_lo(ones, 0u)); }
; __device__ __forceinline__ unsigned xb_ld(unsigned* p)              { return __hip_atomic_load(p, __ATOMIC_RELAXED, __HIP_MEMORY_SCOPE_AGENT); }
; __device__ __forceinline__ unsigned xb_add(unsigned* p, unsigned v) { return __hip_atomic_fetch_add(p, v, __ATOMIC_RELAXED, __HIP_MEMORY_SCOPE_AGENT); }
; __device__ __forceinline__ unsigned xb_xcc_id() { return (unsigned)__builtin_amdgcn_s_getreg((3 << 11) | 20) & 0xFu; }
; #define XB_SPIN(cond, bar) do { unsigned _sp = 0; while (cond) { __builtin_amdgcn_s_sleep(1); \
;     if ((++_sp & 255u) == 0u) { if (xb_ld(&(bar)[XB_TMO])) break; if (_sp > XB_SPIN_CAP) { atomicAdd(&(bar)[XB_TMO], 1u); break; } } } } while (0)
; __device__ __forceinline__ void xcd_barrier(const XcdBarrier& b, int wave_s) {
;     ...
;     if (wave_s == 0 && lane_id() == 0) {
;         unsigned* bar = b.bar; asm volatile("" : "+s"(bar));
;         const unsigned bx_ = xb_xcc_id();
;         __builtin_amdgcn_s_waitcnt(0);
;         unsigned nloc = b.st[0], nx = b.st[1];
;         if (nloc == 0u) { xcd_barrier_complete(bar, bx_, nloc, nx); b.st[0] = nloc; b.st[1] = nx; }
;         const unsigned old = xb_add(&bar[XB_XSUB(bx_)], 1u);
;         const unsigned gen = old / nloc;
;         if (old + 1u == (gen + 1u) * nloc) {
;             __builtin_amdgcn_fence(__ATOMIC_RELEASE, "agent");
;             asm volatile("s_waitcnt vmcnt(0)" ::: "memory");
;             const unsigned og = xb_add(&bar[XB_TOP], 1u);
;             const unsigned tg = og / nx;
;             if (og + 1u == (tg + 1u) * nx) xb_add(&bar[XB_TOPGEN], 1u);
;             else XB_SPIN(xb_ld(&bar[XB_TOPGEN]) == tg, bar);
;             __builtin_amdgcn_fence(__ATOMIC_ACQUIRE, "agent");
;             xb_add(&bar[XB_XGEN(bx_)], 1u);
;             asm volatile("s_waitcnt vmcnt(0)" ::: "memory");
;         } else {
;             XB_SPIN(xb_ld(&bar[XB_XGEN(bx_)]) == gen, bar);
.LBB0_171:
	s_lshl_b32 s2, s33, 8
	s_add_u32 s23, s46, s2
	s_addc_u32 s22, s47, 0
	v_mov_b32_e32 v1, s23
	v_add_co_u32_e32 v4, vcc, 0x1000, v1
	v_mov_b32_e32 v1, s22
	s_nop 0
	v_addc_co_u32_e32 v5, vcc, 0, v1, vcc
	flat_atomic_add v1, v[4:5], v203 offset:1024 sc0
	v_cvt_f32_u32_e32 v3, v2
	v_sub_u32_e32 v4, 0, v2
	v_rcp_iflag_f32_e32 v3, v3
	s_nop 0
	v_mul_f32_e32 v3, 0x4f7ffffe, v3
	v_cvt_u32_f32_e32 v3, v3
	v_mul_lo_u32 v4, v4, v3
	v_mul_hi_u32 v4, v3, v4
	v_add_u32_e32 v3, v3, v4
	s_waitcnt vmcnt(0) lgkmcnt(0)
	v_mul_hi_u32 v3, v1, v3
	v_mul_lo_u32 v5, v3, v2
	v_add_u32_e32 v4, 1, v1
	v_sub_u32_e32 v1, v1, v5
	v_add_u32_e32 v6, 1, v3
	v_cmp_ge_u32_e32 vcc, v1, v2
	v_sub_u32_e32 v5, v1, v2
	s_nop 0
	v_cndmask_b32_e32 v3, v3, v6, vcc
	v_cndmask_b32_e32 v1, v1, v5, vcc
	v_add_u32_e32 v5, 1, v3
	v_cmp_ge_u32_e32 vcc, v1, v2
	s_nop 1
	v_cndmask_b32_e32 v1, v3, v5, vcc
	v_mad_u64_u32 v[2:3], s[2:3], v2, v1, v[2:3]
	v_cmp_ne_u32_e32 vcc, v4, v2
	s_and_saveexec_b64 s[2:3], vcc
	s_xor_b64 s[2:3], exec, s[2:3]
	s_cbranch_execz .LBB0_184
	v_mov_b32_e32 v0, s46
	v_add_co_u32_e32 v2, vcc, 0x3100, v0
	v_mov_b32_e32 v0, s47
	s_nop 0
	v_addc_co_u32_e32 v3, vcc, 0, v0, vcc
	flat_load_dword v0, v[2:3] offset:1024 sc1
	s_add_u32 s6, s46, 0x3500
	s_addc_u32 s7, s47, 0
	s_waitcnt vmcnt(0) lgkmcnt(0)
	v_cmp_eq_u32_e32 vcc, v0, v1
	s_and_saveexec_b64 s[4:5], vcc
	s_cbranch_execz .LBB0_183
	s_mov_b32 s24, 1
	s_mov_b64 s[8:9], 0
	s_branch .LBB0_175

; __device__ __forceinline__ unsigned xb_ld(unsigned* p)              { return __hip_atomic_load(p, __ATOMIC_RELAXED, __HIP_MEMORY_SCOPE_AGENT); }
; __device__ __forceinline__ unsigned xb_add(unsigned* p, unsigned v) { return __hip_atomic_fetch_add(p, v, __ATOMIC_RELAXED, __HIP_MEMORY_SCOPE_AGENT); }
; #define XB_SPIN(cond, bar) do { unsigned _sp = 0; while (cond) { __builtin_amdgcn_s_sleep(1); \
;     if ((++_sp & 255u) == 0u) { if (xb_ld(&(bar)[XB_TMO])) break; if (_sp > XB_SPIN_CAP) { atomicAdd(&(bar)[XB_TMO], 1u); break; } } } } while (0)
; __device__ __forceinline__ void xcd_barrier(const XcdBarrier& b, int wave_s) {
;     ...
;         if (old + 1u == (gen + 1u) * nloc) {
;             __builtin_amdgcn_fence(__ATOMIC_RELEASE, "agent");
;             asm volatile("s_waitcnt vmcnt(0)" ::: "memory");
;             const unsigned og = xb_add(&bar[XB_TOP], 1u);
;             const unsigned tg = og / nx;
;             if (og + 1u == (tg + 1u) * nx) xb_add(&bar[XB_TOPGEN], 1u);
;             else XB_SPIN(xb_ld(&bar[XB_TOPGEN]) == tg, bar);
;             __builtin_amdgcn_fence(__ATOMIC_ACQUIRE, "agent");
;             xb_add(&bar[XB_XGEN(bx_)], 1u);
;             asm volatile("s_waitcnt vmcnt(0)" ::: "memory");
.LBB0_199:
	s_or_b64 exec, exec, s[2:3]
	v_mov_b32_e32 v0, s23
	v_add_co_u32_e32 v0, vcc, 0x2000, v0
	v_mov_b32_e32 v1, s22
	s_nop 0
	v_addc_co_u32_e32 v1, vcc, 0, v1, vcc
	s_waitcnt vmcnt(0) lgkmcnt(0)
	buffer_inv sc1
.LBB0_200:
	s_or_b64 exec, exec, s[40:41]

; __device__ __forceinline__ int lane_id() { unsigned ones = ~0u; asm volatile("" : "+s"(ones)); return (int)__builtin_amdgcn_mbcnt_hi(ones, __builtin_amdgcn_mbcnt_lo(ones, 0u)); }
; __device__ __forceinline__ unsigned xb_ld(unsigned* p)              { return __hip_atomic_load(p, __ATOMIC_RELAXED, __HIP_MEMORY_SCOPE_AGENT); }
; __device__ __forceinline__ unsigned xb_add(unsigned* p, unsigned v) { return __hip_atomic_fetch_add(p, v, __ATOMIC_RELAXED, __HIP_MEMORY_SCOPE_AGENT); }
; __device__ __forceinline__ unsigned xb_xcc_id() { return (unsigned)__builtin_amdgcn_s_getreg((3 << 11) | 20) & 0xFu; }
; #define XB_SPIN(cond, bar) do { unsigned _sp = 0; while (cond) { __builtin_amdgcn_s_sleep(1); \
;     if ((++_sp & 255u) == 0u) { if (xb_ld(&(bar)[XB_TMO])) break; if (_sp > XB_SPIN_CAP) { atomicAdd(&(bar)[XB_TMO], 1u); break; } } } } while (0)
; __device__ __forceinline__ void xcd_barrier(const XcdBarrier& b, int wave_s) {
;     ...
;     if (wave_s == 0 && lane_id() == 0) {
;         unsigned* bar = b.bar; asm volatile("" : "+s"(bar));
;         const unsigned bx_ = xb_xcc_id();
;         __builtin_amdgcn_s_waitcnt(0);
;         unsigned nloc = b.st[0], nx = b.st[1];
;         if (nloc == 0u) { xcd_barrier_complete(bar, bx_, nloc, nx); b.st[0] = nloc; b.st[1] = nx; }
;         const unsigned old = xb_add(&bar[XB_XSUB(bx_)], 1u);
;         const unsigned gen = old / nloc;
;         if (old + 1u == (gen + 1u) * nloc) {
;             __builtin_amdgcn_fence(__ATOMIC_RELEASE, "agent");
;             asm volatile("s_waitcnt vmcnt(0)" ::: "memory");
;             const unsigned og = xb_add(&bar[XB_TOP], 1u);
;             const unsigned tg = og / nx;
;             if (og + 1u == (tg + 1u) * nx) xb_add(&bar[XB_TOPGEN], 1u);
;             else XB_SPIN(xb_ld(&bar[XB_TOPGEN]) == tg, bar);
;             __builtin_amdgcn_fence(__ATOMIC_ACQUIRE, "agent");
;             xb_add(&bar[XB_XGEN(bx_)], 1u);
;             asm volatile("s_waitcnt vmcnt(0)" ::: "memory");
;         } else {
;             XB_SPIN(xb_ld(&bar[XB_XGEN(bx_)]) == gen, bar);
.LBB0_385:
	s_lshl_b32 s2, s33, 8
	s_add_u32 s23, s46, s2
	s_addc_u32 s22, s47, 0
	v_mov_b32_e32 v1, s23
	v_add_co_u32_e32 v4, vcc, 0x1000, v1
	v_mov_b32_e32 v1, s22
	s_nop 0
	v_addc_co_u32_e32 v5, vcc, 0, v1, vcc
	flat_atomic_add v3, v[4:5], v203 offset:1024 sc0
	v_cvt_f32_u32_e32 v1, v2
	v_sub_u32_e32 v4, 0, v2
	v_rcp_iflag_f32_e32 v1, v1
	s_nop 0
	v_mul_f32_e32 v1, 0x4f7ffffe, v1
	v_cvt_u32_f32_e32 v1, v1
	v_mul_lo_u32 v4, v4, v1
	v_mul_hi_u32 v4, v1, v4
	v_add_u32_e32 v1, v1, v4
	s_waitcnt vmcnt(0) lgkmcnt(0)
	v_mul_hi_u32 v1, v3, v1
	v_mul_lo_u32 v4, v1, v2
	v_sub_u32_e32 v4, v3, v4
	v_cmp_ge_u32_e32 vcc, v4, v2
	v_add_u32_e32 v5, 1, v1
	s_nop 0
	v_cndmask_b32_e32 v1, v1, v5, vcc
	v_sub_u32_e32 v5, v4, v2
	v_cndmask_b32_e32 v4, v4, v5, vcc
	v_cmp_ge_u32_e32 vcc, v4, v2
	v_add_u32_e32 v4, 1, v1
	s_nop 0
	v_cndmask_b32_e32 v1, v1, v4, vcc
	v_add_u32_e32 v4, 1, v3
	v_mad_u64_u32 v[2:3], s[2:3], v2, v1, v[2:3]
	v_cmp_ne_u32_e32 vcc, v4, v2
	s_and_saveexec_b64 s[2:3], vcc
	s_xor_b64 s[2:3], exec, s[2:3]
	s_cbranch_execz .LBB0_398
	v_mov_b32_e32 v0, s46
	v_add_co_u32_e32 v2, vcc, 0x3100, v0
	v_mov_b32_e32 v0, s47
	s_nop 0
	v_addc_co_u32_e32 v3, vcc, 0, v0, vcc
	flat_load_dword v0, v[2:3] offset:1024 sc1
	s_add_u32 s6, s46, 0x3500
	s_addc_u32 s7, s47, 0
	s_waitcnt vmcnt(0) lgkmcnt(0)
	v_cmp_eq_u32_e32 vcc, v0, v1
	s_and_saveexec_b64 s[4:5], vcc
	s_cbranch_execz .LBB0_397
	s_mov_b32 s24, 1
	s_mov_b64 s[8:9], 0
	s_branch .LBB0_389

; __device__ __forceinline__ unsigned xb_ld(unsigned* p)              { return __hip_atomic_load(p, __ATOMIC_RELAXED, __HIP_MEMORY_SCOPE_AGENT); }
; __device__ __forceinline__ unsigned xb_add(unsigned* p, unsigned v) { return __hip_atomic_fetch_add(p, v, __ATOMIC_RELAXED, __HIP_MEMORY_SCOPE_AGENT); }
; #define XB_SPIN(cond, bar) do { unsigned _sp = 0; while (cond) { __builtin_amdgcn_s_sleep(1); \
;     if ((++_sp & 255u) == 0u) { if (xb_ld(&(bar)[XB_TMO])) break; if (_sp > XB_SPIN_CAP) { atomicAdd(&(bar)[XB_TMO], 1u); break; } } } } while (0)
; __device__ __forceinline__ void xcd_barrier(const XcdBarrier& b, int wave_s) {
;     ...
;         if (old + 1u == (gen + 1u) * nloc) {
;             __builtin_amdgcn_fence(__ATOMIC_RELEASE, "agent");
;             asm volatile("s_waitcnt vmcnt(0)" ::: "memory");
;             const unsigned og = xb_add(&bar[XB_TOP], 1u);
;             const unsigned tg = og / nx;
;             if (og + 1u == (tg + 1u) * nx) xb_add(&bar[XB_TOPGEN], 1u);
;             else XB_SPIN(xb_ld(&bar[XB_TOPGEN]) == tg, bar);
;             __builtin_amdgcn_fence(__ATOMIC_ACQUIRE, "agent");
;             xb_add(&bar[XB_XGEN(bx_)], 1u);
;             asm volatile("s_waitcnt vmcnt(0)" ::: "memory");
.LBB0_413:
	s_or_b64 exec, exec, s[2:3]
	v_mov_b32_e32 v0, s23
	v_add_co_u32_e32 v0, vcc, 0x2000, v0
	v_mov_b32_e32 v1, s22
	s_nop 0
	v_addc_co_u32_e32 v1, vcc, 0, v1, vcc
	s_waitcnt vmcnt(0) lgkmcnt(0)
	buffer_inv sc1
.LBB0_414:
	s_or_b64 exec, exec, s[40:41]

; __device__ __forceinline__ unsigned xb_ld(unsigned* p)              { return __hip_atomic_load(p, __ATOMIC_RELAXED, __HIP_MEMORY_SCOPE_AGENT); }
; __device__ __forceinline__ unsigned xb_add(unsigned* p, unsigned v) { return __hip_atomic_fetch_add(p, v, __ATOMIC_RELAXED, __HIP_MEMORY_SCOPE_AGENT); }
; #define XB_SPIN(cond, bar) do { unsigned _sp = 0; while (cond) { __builtin_amdgcn_s_sleep(1); \
;     if ((++_sp & 255u) == 0u) { if (xb_ld(&(bar)[XB_TMO])) break; if (_sp > XB_SPIN_CAP) { atomicAdd(&(bar)[XB_TMO], 1u); break; } } } } while (0)
; __device__ __forceinline__ void xcd_barrier(const XcdBarrier& b, int wave_s) {
;     ...
;         if (old + 1u == (gen + 1u) * nloc) {
;             __builtin_amdgcn_fence(__ATOMIC_RELEASE, "agent");
;             asm volatile("s_waitcnt vmcnt(0)" ::: "memory");
;             const unsigned og = xb_add(&bar[XB_TOP], 1u);
;             const unsigned tg = og / nx;
;             if (og + 1u == (tg + 1u) * nx) xb_add(&bar[XB_TOPGEN], 1u);
;             else XB_SPIN(xb_ld(&bar[XB_TOPGEN]) == tg, bar);
;             __builtin_amdgcn_fence(__ATOMIC_ACQUIRE, "agent");
;             xb_add(&bar[XB_XGEN(bx_)], 1u);
;             asm volatile("s_waitcnt vmcnt(0)" ::: "memory");
.LBB0_479:
	s_or_b64 exec, exec, s[2:3]
	v_mov_b32_e32 v0, s23
	v_add_co_u32_e32 v0, vcc, 0x2000, v0
	v_mov_b32_e32 v1, s22
	s_nop 0
	v_addc_co_u32_e32 v1, vcc, 0, v1, vcc
	s_waitcnt vmcnt(0) lgkmcnt(0)
	buffer_inv sc1
.LBB0_480:
	s_or_b64 exec, exec, s[40:41]

; __device__ __forceinline__ int lane_id() { unsigned ones = ~0u; asm volatile("" : "+s"(ones)); return (int)__builtin_amdgcn_mbcnt_hi(ones, __builtin_amdgcn_mbcnt_lo(ones, 0u)); }
; __device__ __forceinline__ unsigned xb_ld(unsigned* p)              { return __hip_atomic_load(p, __ATOMIC_RELAXED, __HIP_MEMORY_SCOPE_AGENT); }
; __device__ __forceinline__ unsigned xb_add(unsigned* p, unsigned v) { return __hip_atomic_fetch_add(p, v, __ATOMIC_RELAXED, __HIP_MEMORY_SCOPE_AGENT); }
; __device__ __forceinline__ unsigned xb_xcc_id() { return (unsigned)__builtin_amdgcn_s_getreg((3 << 11) | 20) & 0xFu; }
; #define XB_SPIN(cond, bar) do { unsigned _sp = 0; while (cond) { __builtin_amdgcn_s_sleep(1); \
;     if ((++_sp & 255u) == 0u) { if (xb_ld(&(bar)[XB_TMO])) break; if (_sp > XB_SPIN_CAP) { atomicAdd(&(bar)[XB_TMO], 1u); break; } } } } while (0)
; __device__ __forceinline__ void xcd_barrier(const XcdBarrier& b, int wave_s) {
;     ...
;     if (wave_s == 0 && lane_id() == 0) {
;         unsigned* bar = b.bar; asm volatile("" : "+s"(bar));
;         const unsigned bx_ = xb_xcc_id();
;         __builtin_amdgcn_s_waitcnt(0);
;         unsigned nloc = b.st[0], nx = b.st[1];
;         if (nloc == 0u) { xcd_barrier_complete(bar, bx_, nloc, nx); b.st[0] = nloc; b.st[1] = nx; }
;         const unsigned old = xb_add(&bar[XB_XSUB(bx_)], 1u);
;         const unsigned gen = old / nloc;
;         if (old + 1u == (gen + 1u) * nloc) {
;             __builtin_amdgcn_fence(__ATOMIC_RELEASE, "agent");
;             asm volatile("s_waitcnt vmcnt(0)" ::: "memory");
;             const unsigned og = xb_add(&bar[XB_TOP], 1u);
;             const unsigned tg = og / nx;
;             if (og + 1u == (tg + 1u) * nx) xb_add(&bar[XB_TOPGEN], 1u);
;             else XB_SPIN(xb_ld(&bar[XB_TOPGEN]) == tg, bar);
;             __builtin_amdgcn_fence(__ATOMIC_ACQUIRE, "agent");
;             xb_add(&bar[XB_XGEN(bx_)], 1u);
;             asm volatile("s_waitcnt vmcnt(0)" ::: "memory");
;         } else {
;             XB_SPIN(xb_ld(&bar[XB_XGEN(bx_)]) == gen, bar);
.LBB0_519:
	s_lshl_b32 s2, s33, 8
	s_add_u32 s23, s76, s2
	s_addc_u32 s22, s77, 0
	v_mov_b32_e32 v1, s23
	v_add_co_u32_e32 v4, vcc, 0x1000, v1
	v_mov_b32_e32 v1, s22
	s_nop 0
	v_addc_co_u32_e32 v5, vcc, 0, v1, vcc
	flat_atomic_add v3, v[4:5], v203 offset:1024 sc0
	v_cvt_f32_u32_e32 v1, v2
	v_sub_u32_e32 v4, 0, v2
	v_rcp_iflag_f32_e32 v1, v1
	s_nop 0
	v_mul_f32_e32 v1, 0x4f7ffffe, v1
	v_cvt_u32_f32_e32 v1, v1
	v_mul_lo_u32 v4, v4, v1
	v_mul_hi_u32 v4, v1, v4
	v_add_u32_e32 v1, v1, v4
	s_waitcnt vmcnt(0) lgkmcnt(0)
	v_mul_hi_u32 v1, v3, v1
	v_mul_lo_u32 v4, v1, v2
	v_sub_u32_e32 v4, v3, v4
	v_cmp_ge_u32_e32 vcc, v4, v2
	v_add_u32_e32 v5, 1, v1
	s_nop 0
	v_cndmask_b32_e32 v1, v1, v5, vcc
	v_sub_u32_e32 v5, v4, v2
	v_cndmask_b32_e32 v4, v4, v5, vcc
	v_cmp_ge_u32_e32 vcc, v4, v2
	v_add_u32_e32 v4, 1, v1
	s_nop 0
	v_cndmask_b32_e32 v1, v1, v4, vcc
	v_add_u32_e32 v4, 1, v3
	v_mad_u64_u32 v[2:3], s[2:3], v2, v1, v[2:3]
	v_cmp_ne_u32_e32 vcc, v4, v2
	s_and_saveexec_b64 s[2:3], vcc
	s_xor_b64 s[2:3], exec, s[2:3]
	s_cbranch_execz .LBB0_532
	v_mov_b32_e32 v0, s76
	v_add_co_u32_e32 v2, vcc, 0x3100, v0
	v_mov_b32_e32 v0, s77
	s_nop 0
	v_addc_co_u32_e32 v3, vcc, 0, v0, vcc
	flat_load_dword v0, v[2:3] offset:1024 sc1
	s_add_u32 s6, s76, 0x3500
	s_addc_u32 s7, s77, 0
	s_waitcnt vmcnt(0) lgkmcnt(0)
	v_cmp_eq_u32_e32 vcc, v0, v1
	s_and_saveexec_b64 s[4:5], vcc
	s_cbranch_execz .LBB0_531
	s_mov_b32 s24, 1
	s_mov_b64 s[8:9], 0
	s_branch .LBB0_523

; __device__ __forceinline__ unsigned xb_ld(unsigned* p)              { return __hip_atomic_load(p, __ATOMIC_RELAXED, __HIP_MEMORY_SCOPE_AGENT); }
; __device__ __forceinline__ unsigned xb_add(unsigned* p, unsigned v) { return __hip_atomic_fetch_add(p, v, __ATOMIC_RELAXED, __HIP_MEMORY_SCOPE_AGENT); }
; #define XB_SPIN(cond, bar) do { unsigned _sp = 0; while (cond) { __builtin_amdgcn_s_sleep(1); \
;     if ((++_sp & 255u) == 0u) { if (xb_ld(&(bar)[XB_TMO])) break; if (_sp > XB_SPIN_CAP) { atomicAdd(&(bar)[XB_TMO], 1u); break; } } } } while (0)
; __device__ __forceinline__ void xcd_barrier(const XcdBarrier& b, int wave_s) {
;     ...
;         if (old + 1u == (gen + 1u) * nloc) {
;             __builtin_amdgcn_fence(__ATOMIC_RELEASE, "agent");
;             asm volatile("s_waitcnt vmcnt(0)" ::: "memory");
;             const unsigned og = xb_add(&bar[XB_TOP], 1u);
;             const unsigned tg = og / nx;
;             if (og + 1u == (tg + 1u) * nx) xb_add(&bar[XB_TOPGEN], 1u);
;             else XB_SPIN(xb_ld(&bar[XB_TOPGEN]) == tg, bar);
;             __builtin_amdgcn_fence(__ATOMIC_ACQUIRE, "agent");
;             xb_add(&bar[XB_XGEN(bx_)], 1u);
;             asm volatile("s_waitcnt vmcnt(0)" ::: "memory");
.LBB0_547:
	s_or_b64 exec, exec, s[2:3]
	v_mov_b32_e32 v0, s23
	v_add_co_u32_e32 v0, vcc, 0x2000, v0
	v_mov_b32_e32 v1, s22
	s_nop 0
	v_addc_co_u32_e32 v1, vcc, 0, v1, vcc
	s_waitcnt vmcnt(0) lgkmcnt(0)
	buffer_inv sc1
.LBB0_548:
	s_or_b64 exec, exec, s[46:47]

; __device__ __forceinline__ unsigned xb_ld(unsigned* p)              { return __hip_atomic_load(p, __ATOMIC_RELAXED, __HIP_MEMORY_SCOPE_AGENT); }
; __device__ __forceinline__ unsigned xb_add(unsigned* p, unsigned v) { return __hip_atomic_fetch_add(p, v, __ATOMIC_RELAXED, __HIP_MEMORY_SCOPE_AGENT); }
; #define XB_SPIN(cond, bar) do { unsigned _sp = 0; while (cond) { __builtin_amdgcn_s_sleep(1); \
;     if ((++_sp & 255u) == 0u) { if (xb_ld(&(bar)[XB_TMO])) break; if (_sp > XB_SPIN_CAP) { atomicAdd(&(bar)[XB_TMO], 1u); break; } } } } while (0)
; __device__ __forceinline__ void xcd_barrier(const XcdBarrier& b, int wave_s) {
;     ...
;         if (old + 1u == (gen + 1u) * nloc) {
;             __builtin_amdgcn_fence(__ATOMIC_RELEASE, "agent");
;             asm volatile("s_waitcnt vmcnt(0)" ::: "memory");
;             const unsigned og = xb_add(&bar[XB_TOP], 1u);
;             const unsigned tg = og / nx;
;             if (og + 1u == (tg + 1u) * nx) xb_add(&bar[XB_TOPGEN], 1u);
;             else XB_SPIN(xb_ld(&bar[XB_TOPGEN]) == tg, bar);
;             __builtin_amdgcn_fence(__ATOMIC_ACQUIRE, "agent");
;             xb_add(&bar[XB_XGEN(bx_)], 1u);
;             asm volatile("s_waitcnt vmcnt(0)" ::: "memory");
.LBB0_631:
	s_or_b64 exec, exec, s[2:3]
	v_mov_b32_e32 v0, s23
	v_add_co_u32_e32 v0, vcc, 0x2000, v0
	v_mov_b32_e32 v1, s22
	s_nop 0
	v_addc_co_u32_e32 v1, vcc, 0, v1, vcc
	s_waitcnt vmcnt(0) lgkmcnt(0)
	buffer_inv sc1
.LBB0_632:
	s_or_b64 exec, exec, s[46:47]

; __device__ __forceinline__ unsigned xb_ld(unsigned* p)              { return __hip_atomic_load(p, __ATOMIC_RELAXED, __HIP_MEMORY_SCOPE_AGENT); }
; __device__ __forceinline__ unsigned xb_add(unsigned* p, unsigned v) { return __hip_atomic_fetch_add(p, v, __ATOMIC_RELAXED, __HIP_MEMORY_SCOPE_AGENT); }
; #define XB_SPIN(cond, bar) do { unsigned _sp = 0; while (cond) { __builtin_amdgcn_s_sleep(1); \
;     if ((++_sp & 255u) == 0u) { if (xb_ld(&(bar)[XB_TMO])) break; if (_sp > XB_SPIN_CAP) { atomicAdd(&(bar)[XB_TMO], 1u); break; } } } } while (0)
; __device__ __forceinline__ void xcd_barrier(const XcdBarrier& b, int wave_s) {
;     ...
;         if (old + 1u == (gen + 1u) * nloc) {
;             __builtin_amdgcn_fence(__ATOMIC_RELEASE, "agent");
;             asm volatile("s_waitcnt vmcnt(0)" ::: "memory");
;             const unsigned og = xb_add(&bar[XB_TOP], 1u);
;             const unsigned tg = og / nx;
;             if (og + 1u == (tg + 1u) * nx) xb_add(&bar[XB_TOPGEN], 1u);
;             else XB_SPIN(xb_ld(&bar[XB_TOPGEN]) == tg, bar);
;             __builtin_amdgcn_fence(__ATOMIC_ACQUIRE, "agent");
;             xb_add(&bar[XB_XGEN(bx_)], 1u);
;             asm volatile("s_waitcnt vmcnt(0)" ::: "memory");
.LBB0_702:
	s_or_b64 exec, exec, s[2:3]
	v_mov_b32_e32 v0, s23
	v_add_co_u32_e32 v0, vcc, 0x2000, v0
	v_mov_b32_e32 v1, s22
	s_nop 0
	v_addc_co_u32_e32 v1, vcc, 0, v1, vcc
	s_waitcnt vmcnt(0) lgkmcnt(0)
	buffer_inv sc1
.LBB0_703:
	s_or_b64 exec, exec, s[40:41]
